# baseline (speedup 1.0000x reference)
.LBB1_7:
	s_and_b64 s[4:5], s[20:21], exec
	s_cselect_b32 s4, s13, s15
	s_cselect_b32 s5, s12, s14
	s_lshr_b32 s6, s3, 11
	s_lshl_b32 s2, s2, 14
	s_and_b32 s2, s2, 0x3c000
	s_lshl_b32 s3, s6, 21
	s_or_b32 s2, s3, s2
	s_add_u32 s7, s5, s2
	s_mov_b32 s3, 0
	s_addc_u32 s8, s4, 0
	s_lshl_b32 s12, s29, 1
	s_lshr_b32 s9, s30, 8
	s_andn2_b64 vcc, exec, s[18:19]
	s_mov_b64 s[4:5], -1
	s_cbranch_vccnz .LBB1_9
	v_and_b32_e32 v20, 15, v0
	s_lshl_b32 s13, s9, 6
	v_or_b32_e32 v2, s13, v20
	s_movk_i32 s15, 0x410
	s_and_b32 s14, s12, 6
	v_mul_lo_u32 v2, v2, s15
	v_add_u32_e32 v34, 0, v2
	s_lshl_b32 s18, s14, 7
	v_and_b32_e32 v22, 48, v0
	s_lshl_b32 s2, s14, 5
	v_add3_u32 v8, v34, s18, v22
	s_add_i32 s2, s2, s9
	ds_read_b128 v[2:5], v8
	s_lshl_b64 s[4:5], s[2:3], 13
	s_add_u32 s4, s7, s4
	s_addc_u32 s5, s8, s5
	v_lshlrev_b32_e32 v24, 6, v20
	v_mov_b32_e32 v25, 0
	v_lshl_add_u64 v[6:7], s[4:5], 0, v[24:25]
	v_mov_b32_e32 v23, v25
	v_lshl_add_u64 v[10:11], v[6:7], 0, v[22:23]
	s_waitcnt lgkmcnt(0)
	global_store_dwordx4 v[10:11], v[2:5], off
	v_or_b32_e32 v10, 16, v20
	ds_read_b128 v[6:9], v8 offset:64
	v_or_b32_e32 v2, s13, v10
	v_mul_lo_u32 v2, v2, s15
	v_add_u32_e32 v35, 0, v2
	v_add3_u32 v12, v35, s18, v22
	ds_read_b128 v[2:5], v12
	v_lshlrev_b32_e32 v26, 6, v10
	v_mov_b32_e32 v27, v25
	v_lshl_add_u64 v[10:11], s[4:5], 0, v[26:27]
	v_lshl_add_u64 v[14:15], v[10:11], 0, v[22:23]
	s_waitcnt lgkmcnt(0)
	global_store_dwordx4 v[14:15], v[2:5], off
	v_or_b32_e32 v14, 32, v20
	ds_read_b128 v[10:13], v12 offset:64
	v_or_b32_e32 v2, s13, v14
	v_mul_lo_u32 v2, v2, s15
	v_add_u32_e32 v36, 0, v2
	v_add3_u32 v16, v36, s18, v22
	ds_read_b128 v[2:5], v16
	v_lshlrev_b32_e32 v28, 6, v14
	v_mov_b32_e32 v29, v25
	v_lshl_add_u64 v[14:15], s[4:5], 0, v[28:29]
	v_lshl_add_u64 v[18:19], v[14:15], 0, v[22:23]
	s_waitcnt lgkmcnt(0)
	global_store_dwordx4 v[18:19], v[2:5], off
	v_or_b32_e32 v18, 48, v20
	ds_read_b128 v[14:17], v16 offset:64
	v_or_b32_e32 v2, s13, v18
	v_mul_lo_u32 v2, v2, s15
	v_add_u32_e32 v37, 0, v2
	v_add3_u32 v20, v37, s18, v22
	ds_read_b128 v[2:5], v20
	v_lshlrev_b32_e32 v30, 6, v18
	v_mov_b32_e32 v31, v25
	v_lshl_add_u64 v[18:19], s[4:5], 0, v[30:31]
	s_add_u32 s4, s4, 0x1000
	v_lshl_add_u64 v[32:33], v[18:19], 0, v[22:23]
	s_addc_u32 s5, s5, 0
	s_waitcnt lgkmcnt(0)
	global_store_dwordx4 v[32:33], v[2:5], off
	ds_read_b128 v[18:21], v20 offset:64
	s_or_b32 s2, s14, 1
	v_lshl_add_u64 v[2:3], s[4:5], 0, v[24:25]
	v_lshl_add_u64 v[2:3], v[2:3], 0, v[22:23]
	global_store_dwordx4 v[2:3], v[6:9], off
	v_lshl_add_u64 v[2:3], s[4:5], 0, v[26:27]
	v_lshl_add_u64 v[2:3], v[2:3], 0, v[22:23]
	global_store_dwordx4 v[2:3], v[10:13], off
	v_lshl_add_u64 v[2:3], s[4:5], 0, v[28:29]
	v_lshl_add_u64 v[2:3], v[2:3], 0, v[22:23]
	global_store_dwordx4 v[2:3], v[14:17], off
	v_lshl_add_u64 v[2:3], s[4:5], 0, v[30:31]
	s_lshl_b32 s4, s2, 7
	s_lshl_b32 s2, s2, 5
	s_add_i32 s2, s2, s9
	v_lshl_add_u64 v[2:3], v[2:3], 0, v[22:23]
	v_add3_u32 v10, v34, s4, v22
	s_lshl_b64 s[2:3], s[2:3], 13
	s_waitcnt lgkmcnt(0)
	global_store_dwordx4 v[2:3], v[18:21], off
	ds_read_b128 v[2:5], v10
	s_add_u32 s2, s7, s2
	s_addc_u32 s3, s8, s3
	v_lshl_add_u64 v[6:7], s[2:3], 0, v[24:25]
	v_add3_u32 v16, v35, s4, v22
	v_lshl_add_u64 v[14:15], v[6:7], 0, v[22:23]
	ds_read_b128 v[6:9], v16
	ds_read_b128 v[10:13], v10 offset:64
	s_waitcnt lgkmcnt(2)
	global_store_dwordx4 v[14:15], v[2:5], off
	v_add3_u32 v18, v36, s4, v22
	v_add3_u32 v34, v37, s4, v22
	v_lshl_add_u64 v[2:3], s[2:3], 0, v[26:27]
	v_lshl_add_u64 v[14:15], v[2:3], 0, v[22:23]
	ds_read_b128 v[2:5], v16 offset:64
	s_waitcnt lgkmcnt(2)
	global_store_dwordx4 v[14:15], v[6:9], off
	ds_read_b128 v[6:9], v18
	v_lshl_add_u64 v[14:15], s[2:3], 0, v[28:29]
	v_lshl_add_u64 v[32:33], v[14:15], 0, v[22:23]
	ds_read_b128 v[14:17], v34
	ds_read_b128 v[18:21], v18 offset:64
	s_mov_b64 s[4:5], 0
	s_waitcnt lgkmcnt(2)
	global_store_dwordx4 v[32:33], v[6:9], off
	s_nop 1
	v_lshl_add_u64 v[6:7], s[2:3], 0, v[30:31]
	s_add_u32 s2, s2, 0x1000
	v_lshl_add_u64 v[32:33], v[6:7], 0, v[22:23]
	s_addc_u32 s3, s3, 0
	s_waitcnt lgkmcnt(1)
	global_store_dwordx4 v[32:33], v[14:17], off
	ds_read_b128 v[6:9], v34 offset:64
	s_nop 0
	v_lshl_add_u64 v[14:15], s[2:3], 0, v[24:25]
	v_lshl_add_u64 v[14:15], v[14:15], 0, v[22:23]
	global_store_dwordx4 v[14:15], v[10:13], off
	s_nop 1
	v_lshl_add_u64 v[10:11], s[2:3], 0, v[26:27]
	v_lshl_add_u64 v[10:11], v[10:11], 0, v[22:23]
	global_store_dwordx4 v[10:11], v[2:5], off
	s_nop 1
	v_lshl_add_u64 v[2:3], s[2:3], 0, v[28:29]
	v_lshl_add_u64 v[2:3], v[2:3], 0, v[22:23]
	s_waitcnt lgkmcnt(1)
	global_store_dwordx4 v[2:3], v[18:21], off
	v_lshl_add_u64 v[2:3], s[2:3], 0, v[30:31]
	v_lshl_add_u64 v[2:3], v[2:3], 0, v[22:23]
	s_waitcnt lgkmcnt(0)
	global_store_dwordx4 v[2:3], v[6:9], off
.LBB1_9:
	s_andn2_b64 vcc, exec, s[4:5]
	s_cbranch_vccnz .LBB1_13
	v_lshl_or_b32 v2, s9, 6, v1
	s_movk_i32 s13, 0x410
	v_mul_lo_u32 v2, v2, s13
	v_add_u32_e32 v22, 0, v2
	s_and_b32 s12, s12, 6
	v_lshl_add_u32 v23, s12, 7, v22
	s_lshl_b32 s2, s12, 5
	ds_read_b128 v[2:5], v23
	ds_read_b128 v[6:9], v23 offset:16
	ds_read_b128 v[10:13], v23 offset:32
	ds_read_b128 v[14:17], v23 offset:48
	s_mov_b32 s3, 0
	s_add_i32 s2, s2, s9
	s_lshl_b64 s[4:5], s[2:3], 13
	s_add_u32 s4, s7, s4
	s_addc_u32 s5, s8, s5
	v_lshlrev_b32_e32 v18, 4, v1
	s_waitcnt lgkmcnt(3)
	global_store_dwordx4 v18, v[2:5], s[4:5]
	s_waitcnt lgkmcnt(2)
	global_store_dwordx4 v18, v[6:9], s[4:5] offset:1024
	s_waitcnt lgkmcnt(1)
	global_store_dwordx4 v18, v[10:13], s[4:5] offset:2048
	s_waitcnt lgkmcnt(0)
	global_store_dwordx4 v18, v[14:17], s[4:5] offset:3072
	ds_read_b128 v[2:5], v23 offset:64
	ds_read_b128 v[6:9], v23 offset:80
	ds_read_b128 v[10:13], v23 offset:96
	ds_read_b128 v[14:17], v23 offset:112
	v_mov_b32_e32 v19, 0
	v_lshl_add_u64 v[20:21], s[4:5], 0, v[18:19]
	s_movk_i32 s4, 0x1000
	v_add_co_u32_e32 v20, vcc, s4, v20
	s_or_b32 s2, s12, 1
	s_nop 0
	v_addc_co_u32_e32 v21, vcc, 0, v21, vcc
	s_waitcnt lgkmcnt(3)
	global_store_dwordx4 v[20:21], v[2:5], off
	s_waitcnt lgkmcnt(2)
	global_store_dwordx4 v[20:21], v[6:9], off offset:1024
	s_waitcnt lgkmcnt(1)
	global_store_dwordx4 v[20:21], v[10:13], off offset:2048
	s_waitcnt lgkmcnt(0)
	global_store_dwordx4 v[20:21], v[14:17], off offset:3072
	v_lshl_add_u32 v22, s2, 7, v22
	s_lshl_b32 s2, s2, 5
	ds_read_b128 v[2:5], v22
	ds_read_b128 v[6:9], v22 offset:16
	ds_read_b128 v[10:13], v22 offset:32
	ds_read_b128 v[14:17], v22 offset:48
	s_add_i32 s2, s2, s9
	s_lshl_b64 s[2:3], s[2:3], 13
	s_add_u32 s2, s7, s2
	s_addc_u32 s3, s8, s3
	s_waitcnt lgkmcnt(3)
	global_store_dwordx4 v18, v[2:5], s[2:3]
	s_waitcnt lgkmcnt(2)
	global_store_dwordx4 v18, v[6:9], s[2:3] offset:1024
	s_waitcnt lgkmcnt(1)
	global_store_dwordx4 v18, v[10:13], s[2:3] offset:2048
	s_waitcnt lgkmcnt(0)
	global_store_dwordx4 v18, v[14:17], s[2:3] offset:3072
	ds_read_b128 v[2:5], v22 offset:64
	ds_read_b128 v[6:9], v22 offset:80
	ds_read_b128 v[10:13], v22 offset:96
	ds_read_b128 v[14:17], v22 offset:112
	v_lshl_add_u64 v[20:21], s[2:3], 0, v[18:19]
	v_add_co_u32_e32 v18, vcc, s4, v20
	s_nop 1
	v_addc_co_u32_e32 v19, vcc, 0, v21, vcc
	s_waitcnt lgkmcnt(3)
	global_store_dwordx4 v[18:19], v[2:5], off
	s_waitcnt lgkmcnt(2)
	global_store_dwordx4 v[18:19], v[6:9], off offset:1024
	s_waitcnt lgkmcnt(1)
	global_store_dwordx4 v[18:19], v[10:13], off offset:2048
	s_waitcnt lgkmcnt(0)
	global_store_dwordx4 v[18:19], v[14:17], off offset:3072
	v_and_b32_e32 v2, 7, v0
	v_lshl_add_u32 v18, v2, 7, 0
	v_lshl_add_u32 v6, v2, 2, 0
	v_lshrrev_b32_e32 v2, 3, v0
	v_mad_u32_u24 v19, v2, s13, v18
	ds_read_b128 v[2:5], v19
	v_add_u32_e32 v20, 0x20800, v6
	ds_read_b128 v[6:9], v19 offset:16
	ds_read_b128 v[10:13], v19 offset:32
	ds_read_b128 v[14:17], v19 offset:48
	ds_read_b128 v[28:31], v19 offset:64
	ds_read_b128 v[32:35], v19 offset:80
	ds_read_b128 v[36:39], v19 offset:96
	ds_read_b128 v[40:43], v19 offset:112
	v_or_b32_e32 v21, 0x200, v0
	v_lshrrev_b32_e32 v21, 3, v21
	v_mad_u32_u24 v18, v21, s13, v18
	ds_read_b128 v[44:47], v18
	ds_read_b128 v[48:51], v18 offset:16
	ds_read_b128 v[52:55], v18 offset:32
	ds_read_b128 v[56:59], v18 offset:48
	s_waitcnt lgkmcnt(8)
	v_fma_mix_f32 v24, v2, v2, 0 op_sel_hi:[1,1,0]
	v_fma_mix_f32 v25, v6, v6, 0 op_sel_hi:[1,1,0]
	v_fma_mix_f32 v26, v10, v10, 0 op_sel_hi:[1,1,0]
	v_fma_mix_f32 v27, v14, v14, 0 op_sel_hi:[1,1,0]
	v_fma_mix_f32 v24, v2, v2, v24 op_sel:[1,1,0] op_sel_hi:[1,1,0]
	v_fma_mix_f32 v25, v6, v6, v25 op_sel:[1,1,0] op_sel_hi:[1,1,0]
	v_fma_mix_f32 v26, v10, v10, v26 op_sel:[1,1,0] op_sel_hi:[1,1,0]
	v_fma_mix_f32 v27, v14, v14, v27 op_sel:[1,1,0] op_sel_hi:[1,1,0]
	v_fma_mix_f32 v24, v3, v3, v24 op_sel_hi:[1,1,0]
	v_fma_mix_f32 v25, v7, v7, v25 op_sel_hi:[1,1,0]
	v_fma_mix_f32 v26, v11, v11, v26 op_sel_hi:[1,1,0]
	v_fma_mix_f32 v27, v15, v15, v27 op_sel_hi:[1,1,0]
	v_fma_mix_f32 v24, v3, v3, v24 op_sel:[1,1,0] op_sel_hi:[1,1,0]
	v_fma_mix_f32 v25, v7, v7, v25 op_sel:[1,1,0] op_sel_hi:[1,1,0]
	v_fma_mix_f32 v26, v11, v11, v26 op_sel:[1,1,0] op_sel_hi:[1,1,0]
	v_fma_mix_f32 v27, v15, v15, v27 op_sel:[1,1,0] op_sel_hi:[1,1,0]
	v_fma_mix_f32 v24, v4, v4, v24 op_sel_hi:[1,1,0]
	v_fma_mix_f32 v25, v8, v8, v25 op_sel_hi:[1,1,0]
	v_fma_mix_f32 v26, v12, v12, v26 op_sel_hi:[1,1,0]
	v_fma_mix_f32 v27, v16, v16, v27 op_sel_hi:[1,1,0]
	v_fma_mix_f32 v24, v4, v4, v24 op_sel:[1,1,0] op_sel_hi:[1,1,0]
	v_fma_mix_f32 v25, v8, v8, v25 op_sel:[1,1,0] op_sel_hi:[1,1,0]
	v_fma_mix_f32 v26, v12, v12, v26 op_sel:[1,1,0] op_sel_hi:[1,1,0]
	v_fma_mix_f32 v27, v16, v16, v27 op_sel:[1,1,0] op_sel_hi:[1,1,0]
	v_fma_mix_f32 v24, v5, v5, v24 op_sel_hi:[1,1,0]
	v_fma_mix_f32 v25, v9, v9, v25 op_sel_hi:[1,1,0]
	v_fma_mix_f32 v26, v13, v13, v26 op_sel_hi:[1,1,0]
	v_fma_mix_f32 v27, v17, v17, v27 op_sel_hi:[1,1,0]
	v_fma_mix_f32 v24, v5, v5, v24 op_sel:[1,1,0] op_sel_hi:[1,1,0]
	v_fma_mix_f32 v25, v9, v9, v25 op_sel:[1,1,0] op_sel_hi:[1,1,0]
	v_fma_mix_f32 v26, v13, v13, v26 op_sel:[1,1,0] op_sel_hi:[1,1,0]
	v_fma_mix_f32 v27, v17, v17, v27 op_sel:[1,1,0] op_sel_hi:[1,1,0]
	ds_read_b128 v[60:63], v18 offset:64
	ds_read_b128 v[64:67], v18 offset:80
	ds_read_b128 v[68:71], v18 offset:96
	ds_read_b128 v[72:75], v18 offset:112
	s_waitcnt lgkmcnt(8)
	v_fma_mix_f32 v24, v28, v28, v24 op_sel_hi:[1,1,0]
	v_fma_mix_f32 v25, v32, v32, v25 op_sel_hi:[1,1,0]
	v_fma_mix_f32 v26, v36, v36, v26 op_sel_hi:[1,1,0]
	v_fma_mix_f32 v27, v40, v40, v27 op_sel_hi:[1,1,0]
	v_fma_mix_f32 v24, v28, v28, v24 op_sel:[1,1,0] op_sel_hi:[1,1,0]
	v_fma_mix_f32 v25, v32, v32, v25 op_sel:[1,1,0] op_sel_hi:[1,1,0]
	v_fma_mix_f32 v26, v36, v36, v26 op_sel:[1,1,0] op_sel_hi:[1,1,0]
	v_fma_mix_f32 v27, v40, v40, v27 op_sel:[1,1,0] op_sel_hi:[1,1,0]
	v_fma_mix_f32 v24, v29, v29, v24 op_sel_hi:[1,1,0]
	v_fma_mix_f32 v25, v33, v33, v25 op_sel_hi:[1,1,0]
	v_fma_mix_f32 v26, v37, v37, v26 op_sel_hi:[1,1,0]
	v_fma_mix_f32 v27, v41, v41, v27 op_sel_hi:[1,1,0]
	v_fma_mix_f32 v24, v29, v29, v24 op_sel:[1,1,0] op_sel_hi:[1,1,0]
	v_fma_mix_f32 v25, v33, v33, v25 op_sel:[1,1,0] op_sel_hi:[1,1,0]
	v_fma_mix_f32 v26, v37, v37, v26 op_sel:[1,1,0] op_sel_hi:[1,1,0]
	v_fma_mix_f32 v27, v41, v41, v27 op_sel:[1,1,0] op_sel_hi:[1,1,0]
	v_fma_mix_f32 v24, v30, v30, v24 op_sel_hi:[1,1,0]
	v_fma_mix_f32 v25, v34, v34, v25 op_sel_hi:[1,1,0]
	v_fma_mix_f32 v26, v38, v38, v26 op_sel_hi:[1,1,0]
	v_fma_mix_f32 v27, v42, v42, v27 op_sel_hi:[1,1,0]
	v_fma_mix_f32 v24, v30, v30, v24 op_sel:[1,1,0] op_sel_hi:[1,1,0]
	v_fma_mix_f32 v25, v34, v34, v25 op_sel:[1,1,0] op_sel_hi:[1,1,0]
	v_fma_mix_f32 v26, v38, v38, v26 op_sel:[1,1,0] op_sel_hi:[1,1,0]
	v_fma_mix_f32 v27, v42, v42, v27 op_sel:[1,1,0] op_sel_hi:[1,1,0]
	v_fma_mix_f32 v24, v31, v31, v24 op_sel_hi:[1,1,0]
	v_fma_mix_f32 v25, v35, v35, v25 op_sel_hi:[1,1,0]
	v_fma_mix_f32 v26, v39, v39, v26 op_sel_hi:[1,1,0]
	v_fma_mix_f32 v27, v43, v43, v27 op_sel_hi:[1,1,0]
	v_fma_mix_f32 v24, v31, v31, v24 op_sel:[1,1,0] op_sel_hi:[1,1,0]
	v_fma_mix_f32 v25, v35, v35, v25 op_sel:[1,1,0] op_sel_hi:[1,1,0]
	v_fma_mix_f32 v26, v39, v39, v26 op_sel:[1,1,0] op_sel_hi:[1,1,0]
	v_fma_mix_f32 v27, v43, v43, v27 op_sel:[1,1,0] op_sel_hi:[1,1,0]
	v_add_f32_e32 v24, v24, v25
	v_add_f32_e32 v26, v26, v27
	s_nop 0
	v_add_f32_e32 v24, v24, v26
	s_nop 0
	ds_max_u32 v20, v24
	s_waitcnt lgkmcnt(5)
	v_fma_mix_f32 v24, v44, v44, 0 op_sel_hi:[1,1,0]
	v_fma_mix_f32 v25, v48, v48, 0 op_sel_hi:[1,1,0]
	v_fma_mix_f32 v26, v52, v52, 0 op_sel_hi:[1,1,0]
	v_fma_mix_f32 v27, v56, v56, 0 op_sel_hi:[1,1,0]
	v_fma_mix_f32 v24, v44, v44, v24 op_sel:[1,1,0] op_sel_hi:[1,1,0]
	v_fma_mix_f32 v25, v48, v48, v25 op_sel:[1,1,0] op_sel_hi:[1,1,0]
	v_fma_mix_f32 v26, v52, v52, v26 op_sel:[1,1,0] op_sel_hi:[1,1,0]
	v_fma_mix_f32 v27, v56, v56, v27 op_sel:[1,1,0] op_sel_hi:[1,1,0]
	v_fma_mix_f32 v24, v45, v45, v24 op_sel_hi:[1,1,0]
	v_fma_mix_f32 v25, v49, v49, v25 op_sel_hi:[1,1,0]
	v_fma_mix_f32 v26, v53, v53, v26 op_sel_hi:[1,1,0]
	v_fma_mix_f32 v27, v57, v57, v27 op_sel_hi:[1,1,0]
	v_fma_mix_f32 v24, v45, v45, v24 op_sel:[1,1,0] op_sel_hi:[1,1,0]
	v_fma_mix_f32 v25, v49, v49, v25 op_sel:[1,1,0] op_sel_hi:[1,1,0]
	v_fma_mix_f32 v26, v53, v53, v26 op_sel:[1,1,0] op_sel_hi:[1,1,0]
	v_fma_mix_f32 v27, v57, v57, v27 op_sel:[1,1,0] op_sel_hi:[1,1,0]
	v_fma_mix_f32 v24, v46, v46, v24 op_sel_hi:[1,1,0]
	v_fma_mix_f32 v25, v50, v50, v25 op_sel_hi:[1,1,0]
	v_fma_mix_f32 v26, v54, v54, v26 op_sel_hi:[1,1,0]
	v_fma_mix_f32 v27, v58, v58, v27 op_sel_hi:[1,1,0]
	v_fma_mix_f32 v24, v46, v46, v24 op_sel:[1,1,0] op_sel_hi:[1,1,0]
	v_fma_mix_f32 v25, v50, v50, v25 op_sel:[1,1,0] op_sel_hi:[1,1,0]
	v_fma_mix_f32 v26, v54, v54, v26 op_sel:[1,1,0] op_sel_hi:[1,1,0]
	v_fma_mix_f32 v27, v58, v58, v27 op_sel:[1,1,0] op_sel_hi:[1,1,0]
	v_fma_mix_f32 v24, v47, v47, v24 op_sel_hi:[1,1,0]
	v_fma_mix_f32 v25, v51, v51, v25 op_sel_hi:[1,1,0]
	v_fma_mix_f32 v26, v55, v55, v26 op_sel_hi:[1,1,0]
	v_fma_mix_f32 v27, v59, v59, v27 op_sel_hi:[1,1,0]
	v_fma_mix_f32 v24, v47, v47, v24 op_sel:[1,1,0] op_sel_hi:[1,1,0]
	v_fma_mix_f32 v25, v51, v51, v25 op_sel:[1,1,0] op_sel_hi:[1,1,0]
	v_fma_mix_f32 v26, v55, v55, v26 op_sel:[1,1,0] op_sel_hi:[1,1,0]
	v_fma_mix_f32 v27, v59, v59, v27 op_sel:[1,1,0] op_sel_hi:[1,1,0]
	s_waitcnt lgkmcnt(1)
	v_fma_mix_f32 v24, v60, v60, v24 op_sel_hi:[1,1,0]
	v_fma_mix_f32 v25, v64, v64, v25 op_sel_hi:[1,1,0]
	v_fma_mix_f32 v26, v68, v68, v26 op_sel_hi:[1,1,0]
	v_fma_mix_f32 v27, v72, v72, v27 op_sel_hi:[1,1,0]
	v_fma_mix_f32 v24, v60, v60, v24 op_sel:[1,1,0] op_sel_hi:[1,1,0]
	v_fma_mix_f32 v25, v64, v64, v25 op_sel:[1,1,0] op_sel_hi:[1,1,0]
	v_fma_mix_f32 v26, v68, v68, v26 op_sel:[1,1,0] op_sel_hi:[1,1,0]
	v_fma_mix_f32 v27, v72, v72, v27 op_sel:[1,1,0] op_sel_hi:[1,1,0]
	v_fma_mix_f32 v24, v61, v61, v24 op_sel_hi:[1,1,0]
	v_fma_mix_f32 v25, v65, v65, v25 op_sel_hi:[1,1,0]
	v_fma_mix_f32 v26, v69, v69, v26 op_sel_hi:[1,1,0]
	v_fma_mix_f32 v27, v73, v73, v27 op_sel_hi:[1,1,0]
	v_fma_mix_f32 v24, v61, v61, v24 op_sel:[1,1,0] op_sel_hi:[1,1,0]
	v_fma_mix_f32 v25, v65, v65, v25 op_sel:[1,1,0] op_sel_hi:[1,1,0]
	v_fma_mix_f32 v26, v69, v69, v26 op_sel:[1,1,0] op_sel_hi:[1,1,0]
	v_fma_mix_f32 v27, v73, v73, v27 op_sel:[1,1,0] op_sel_hi:[1,1,0]
	v_fma_mix_f32 v24, v62, v62, v24 op_sel_hi:[1,1,0]
	v_fma_mix_f32 v25, v66, v66, v25 op_sel_hi:[1,1,0]
	v_fma_mix_f32 v26, v70, v70, v26 op_sel_hi:[1,1,0]
	v_fma_mix_f32 v27, v74, v74, v27 op_sel_hi:[1,1,0]
	v_fma_mix_f32 v24, v62, v62, v24 op_sel:[1,1,0] op_sel_hi:[1,1,0]
	v_fma_mix_f32 v25, v66, v66, v25 op_sel:[1,1,0] op_sel_hi:[1,1,0]
	v_fma_mix_f32 v26, v70, v70, v26 op_sel:[1,1,0] op_sel_hi:[1,1,0]
	v_fma_mix_f32 v27, v74, v74, v27 op_sel:[1,1,0] op_sel_hi:[1,1,0]
	v_fma_mix_f32 v24, v63, v63, v24 op_sel_hi:[1,1,0]
	v_fma_mix_f32 v25, v67, v67, v25 op_sel_hi:[1,1,0]
	v_fma_mix_f32 v26, v71, v71, v26 op_sel_hi:[1,1,0]
	v_fma_mix_f32 v27, v75, v75, v27 op_sel_hi:[1,1,0]
	v_fma_mix_f32 v24, v63, v63, v24 op_sel:[1,1,0] op_sel_hi:[1,1,0]
	v_fma_mix_f32 v25, v67, v67, v25 op_sel:[1,1,0] op_sel_hi:[1,1,0]
	v_fma_mix_f32 v26, v71, v71, v26 op_sel:[1,1,0] op_sel_hi:[1,1,0]
	v_fma_mix_f32 v27, v75, v75, v27 op_sel:[1,1,0] op_sel_hi:[1,1,0]
	v_add_f32_e32 v24, v24, v25
	v_add_f32_e32 v26, v26, v27
	s_nop 0
	v_add_f32_e32 v24, v24, v26
	s_nop 0
	ds_max_u32 v20, v24
	s_waitcnt lgkmcnt(0)
	s_barrier
	s_and_saveexec_b64 s[2:3], s[0:1]
	s_cbranch_execz .LBB1_12
	v_lshlrev_b32_e32 v0, 2, v0
	v_add_u32_e32 v2, 0, v0
	v_add_u32_e32 v2, 0x20800, v2
	ds_read_b32 v2, v2
	s_lshl_b32 s0, s6, 5
	s_add_u32 s0, s16, s0
	s_addc_u32 s1, s17, 0
	s_waitcnt lgkmcnt(0)
	global_atomic_umax v0, v2, s[0:1]

.LBB1_14:
	s_lshl_b32 s4, s29, 4
	v_lshlrev_b32_e32 v0, 4, v1
	s_mov_b32 s1, 0
	v_mov_b32_e32 v1, 0
	s_add_i32 s0, s4, s28
	v_lshl_add_u64 v[8:9], s[10:11], 0, v[0:1]
	s_lshl_b64 s[2:3], s[0:1], 10
	v_add_u32_e32 v4, 0, v0
	s_mulk_i32 s29, 0x4100
	v_lshl_add_u64 v[10:11], v[8:9], 0, s[2:3]
	s_or_b32 s2, s4, 1
	v_add_u32_e32 v0, s29, v4
	s_mul_i32 s3, s2, 0x410
	ds_read_b128 v[0:3], v0
	v_add_u32_e32 v12, s3, v4
	ds_read_b128 v[4:7], v12
	s_add_i32 s2, s2, s28
	s_mov_b32 s3, s1
	s_lshl_b64 s[2:3], s[2:3], 10
	s_waitcnt lgkmcnt(1)
	global_store_dwordx4 v[10:11], v[0:3], off
	s_nop 1
	v_lshl_add_u64 v[0:1], v[8:9], 0, s[2:3]
	s_waitcnt lgkmcnt(0)
	global_store_dwordx4 v[0:1], v[4:7], off
	ds_read_b128 v[0:3], v12 offset:1040
	ds_read_b128 v[4:7], v12 offset:2080
	s_add_i32 s2, s0, 2
	s_mov_b32 s3, s1
	s_lshl_b64 s[2:3], s[2:3], 10
	v_lshl_add_u64 v[10:11], v[8:9], 0, s[2:3]
	s_add_i32 s2, s0, 3
	s_mov_b32 s3, s1
	s_lshl_b64 s[2:3], s[2:3], 10
	s_waitcnt lgkmcnt(1)
	global_store_dwordx4 v[10:11], v[0:3], off
	s_nop 1
	v_lshl_add_u64 v[0:1], v[8:9], 0, s[2:3]
	s_waitcnt lgkmcnt(0)
	global_store_dwordx4 v[0:1], v[4:7], off
	ds_read_b128 v[0:3], v12 offset:3120
	ds_read_b128 v[4:7], v12 offset:4160
	s_add_i32 s2, s0, 4
	s_mov_b32 s3, s1
	s_lshl_b64 s[2:3], s[2:3], 10
	v_lshl_add_u64 v[10:11], v[8:9], 0, s[2:3]
	s_add_i32 s2, s0, 5
	s_mov_b32 s3, s1
	s_lshl_b64 s[2:3], s[2:3], 10
	s_waitcnt lgkmcnt(1)
	global_store_dwordx4 v[10:11], v[0:3], off
	s_nop 1
	v_lshl_add_u64 v[0:1], v[8:9], 0, s[2:3]
	s_waitcnt lgkmcnt(0)
	global_store_dwordx4 v[0:1], v[4:7], off
	ds_read_b128 v[0:3], v12 offset:5200
	ds_read_b128 v[4:7], v12 offset:6240
	s_add_i32 s2, s0, 6
	s_mov_b32 s3, s1
	s_lshl_b64 s[2:3], s[2:3], 10
	v_lshl_add_u64 v[10:11], v[8:9], 0, s[2:3]
	s_add_i32 s2, s0, 7
	s_mov_b32 s3, s1
	s_lshl_b64 s[2:3], s[2:3], 10
	s_waitcnt lgkmcnt(1)
	global_store_dwordx4 v[10:11], v[0:3], off
	s_nop 1
	v_lshl_add_u64 v[0:1], v[8:9], 0, s[2:3]
	s_waitcnt lgkmcnt(0)
	global_store_dwordx4 v[0:1], v[4:7], off
	ds_read_b128 v[0:3], v12 offset:7280
	ds_read_b128 v[4:7], v12 offset:8320
	s_add_i32 s2, s0, 8
	s_mov_b32 s3, s1
	s_lshl_b64 s[2:3], s[2:3], 10
	v_lshl_add_u64 v[10:11], v[8:9], 0, s[2:3]
	s_add_i32 s2, s0, 9
	s_mov_b32 s3, s1
	s_lshl_b64 s[2:3], s[2:3], 10
	s_waitcnt lgkmcnt(1)
	global_store_dwordx4 v[10:11], v[0:3], off
	s_nop 1
	v_lshl_add_u64 v[0:1], v[8:9], 0, s[2:3]
	s_waitcnt lgkmcnt(0)
	global_store_dwordx4 v[0:1], v[4:7], off
	ds_read_b128 v[0:3], v12 offset:9360
	ds_read_b128 v[4:7], v12 offset:10400
	s_add_i32 s2, s0, 10
	s_mov_b32 s3, s1
	s_lshl_b64 s[2:3], s[2:3], 10
	v_lshl_add_u64 v[10:11], v[8:9], 0, s[2:3]
	s_add_i32 s2, s0, 11
	s_mov_b32 s3, s1
	s_lshl_b64 s[2:3], s[2:3], 10
	s_waitcnt lgkmcnt(1)
	global_store_dwordx4 v[10:11], v[0:3], off
	s_nop 1
	v_lshl_add_u64 v[0:1], v[8:9], 0, s[2:3]
	s_waitcnt lgkmcnt(0)
	global_store_dwordx4 v[0:1], v[4:7], off
	ds_read_b128 v[0:3], v12 offset:11440
	ds_read_b128 v[4:7], v12 offset:12480
	s_add_i32 s2, s0, 12
	s_mov_b32 s3, s1
	s_lshl_b64 s[2:3], s[2:3], 10
	v_lshl_add_u64 v[10:11], v[8:9], 0, s[2:3]
	s_add_i32 s2, s0, 13
	s_mov_b32 s3, s1
	s_lshl_b64 s[2:3], s[2:3], 10
	s_waitcnt lgkmcnt(1)
	global_store_dwordx4 v[10:11], v[0:3], off
	s_nop 1
	v_lshl_add_u64 v[0:1], v[8:9], 0, s[2:3]
	s_waitcnt lgkmcnt(0)
	global_store_dwordx4 v[0:1], v[4:7], off
	ds_read_b128 v[0:3], v12 offset:13520
	ds_read_b128 v[4:7], v12 offset:14560
	s_add_i32 s2, s0, 14
	s_mov_b32 s3, s1
	s_lshl_b64 s[2:3], s[2:3], 10
	s_add_i32 s0, s0, 15
	v_lshl_add_u64 v[10:11], v[8:9], 0, s[2:3]
	s_lshl_b64 s[0:1], s[0:1], 10
	s_waitcnt lgkmcnt(1)
	global_store_dwordx4 v[10:11], v[0:3], off
	s_nop 1
	v_lshl_add_u64 v[0:1], v[8:9], 0, s[0:1]
	s_waitcnt lgkmcnt(0)
	global_store_dwordx4 v[0:1], v[4:7], off
	s_endpgm
